# baseline (speedup 1.0000x reference)
.LBB2_1:
	s_mov_b32 s17, s31
	s_mov_b32 s18, s15
	v_add_u32_e32 v196, s18, v192
	ds_read_b64_tr_b16 v[176:177], v196 offset:24576
	ds_read_b64_tr_b16 v[178:179], v196 offset:25088
	s_waitcnt lgkmcnt(9)
	v_mfma_f32_32x32x16_f16 v[96:111], v[172:175], v[136:139], v[0:15]
	v_add_f32_e32 v80, v64, v65
	v_add_f32_e32 v80, v66, v80
	v_add_f32_e32 v80, v67, v80
	v_add_f32_e32 v80, v68, v80
	v_add_f32_e32 v80, v69, v80
	v_cvt_pk_f16_f32 v140, v64, v65
	v_cvt_pk_f16_f32 v141, v66, v67
	ds_read_b64_tr_b16 v[172:173], v196 offset:28672
	ds_read_b64_tr_b16 v[174:175], v196 offset:29184
	v_add_f32_e32 v64, v70, v80
	s_waitcnt lgkmcnt(10)
	v_mfma_f32_32x32x16_f16 v[80:95], v[168:171], v[136:139], v[0:15]
	v_add_f32_e32 v64, v71, v64
	v_add_f32_e32 v64, v72, v64
	v_add_f32_e32 v64, v73, v64
	v_cvt_pk_f16_f32 v142, v68, v69
	v_cvt_pk_f16_f32 v143, v70, v71
	ds_read_b64_tr_b16 v[68:69], v196 offset:25600
	ds_read_b64_tr_b16 v[70:71], v196 offset:26112
	s_waitcnt lgkmcnt(11)
	v_mfma_f32_32x32x16_f16 v[96:111], v[164:167], v[128:131], v[96:111]
	v_add_f32_e32 v64, v74, v64
	v_add_f32_e32 v64, v75, v64
	v_add_f32_e32 v64, v76, v64
	v_add_f32_e32 v116, v77, v64
	v_cvt_pk_f16_f32 v132, v72, v73
	v_cvt_pk_f16_f32 v133, v74, v75
	ds_read_b64_tr_b16 v[64:65], v196 offset:29696
	ds_read_b64_tr_b16 v[66:67], v196 offset:30208
	s_waitcnt lgkmcnt(12)
	v_mfma_f32_32x32x16_f16 v[80:95], v[160:163], v[128:131], v[80:95]
	v_add_f32_e32 v72, v78, v116
	v_add_f32_e32 v72, v79, v72
	v_add_f32_e32 v72, v48, v72
	v_add_f32_e32 v116, v49, v72
	v_cvt_pk_f16_f32 v134, v76, v77
	v_cvt_pk_f16_f32 v135, v78, v79
	ds_read_b64_tr_b16 v[72:73], v196 offset:26624
	ds_read_b64_tr_b16 v[74:75], v196 offset:27136
	s_waitcnt lgkmcnt(13)
	v_mfma_f32_32x32x16_f16 v[96:111], v[156:159], v[120:123], v[96:111]
	v_add_f32_e32 v76, v50, v116
	v_add_f32_e32 v76, v51, v76
	v_add_f32_e32 v76, v52, v76
	v_add_f32_e32 v76, v53, v76
	v_cvt_pk_f16_f32 v124, v48, v49
	v_cvt_pk_f16_f32 v125, v50, v51
	ds_read_b64_tr_b16 v[48:49], v196 offset:30720
	ds_read_b64_tr_b16 v[50:51], v196 offset:31232
	s_waitcnt lgkmcnt(14)
	v_mfma_f32_32x32x16_f16 v[80:95], v[152:155], v[120:123], v[80:95]
	v_add_f32_e32 v76, v54, v76
	v_add_f32_e32 v76, v55, v76
	v_add_f32_e32 v76, v56, v76
	v_add_f32_e32 v76, v57, v76
	v_cvt_pk_f16_f32 v126, v52, v53
	v_cvt_pk_f16_f32 v127, v54, v55
	ds_read_b64_tr_b16 v[52:53], v196 offset:27648
	ds_read_b64_tr_b16 v[54:55], v196 offset:28160
	s_waitcnt lgkmcnt(14)
	v_mfma_f32_32x32x16_f16 v[96:111], v[148:151], v[112:115], v[96:111]
	v_add_f32_e32 v76, v58, v76
	v_add_f32_e32 v76, v59, v76
	v_add_f32_e32 v76, v60, v76
	v_add_f32_e32 v76, v61, v76
	v_cvt_pk_f16_f32 v116, v56, v57
	v_cvt_pk_f16_f32 v117, v58, v59
	ds_read_b64_tr_b16 v[56:57], v196 offset:31744
	ds_read_b64_tr_b16 v[58:59], v196 offset:32256
	v_mfma_f32_32x32x16_f16 v[80:95], v[144:147], v[112:115], v[80:95]
	v_add_f32_e32 v76, v62, v76
	v_add_f32_e32 v76, v63, v76
	v_cvt_pk_f16_f32 v118, v60, v61
	v_cvt_pk_f16_f32 v119, v62, v63
	v_lshl_add_u64 v[60:61], v[182:183], 0, s[12:13]
	s_add_i32 m0, s14, s25
	v_cmp_lt_f32_e32 vcc, s36, v76
	global_load_lds_dwordx4 v[60:61], off
	s_add_i32 m0, s28, s26
	s_nop 0
	global_load_lds_dwordx4 v[180:181], off
	s_cbranch_vccnz .Lmy_rare_1

.LBB2_4:
	v_add_u32_e32 v196, s17, v192
	ds_read_b64_tr_b16 v[144:145], v196 offset:24576
	ds_read_b64_tr_b16 v[146:147], v196 offset:25088
	s_waitcnt lgkmcnt(9)
	v_mfma_f32_32x32x16_f16 v[64:79], v[60:63], v[136:139], v[0:15]
	v_add_f32_e32 v48, v96, v97
	v_add_f32_e32 v48, v98, v48
	v_add_f32_e32 v48, v99, v48
	v_add_f32_e32 v48, v100, v48
	v_add_f32_e32 v48, v101, v48
	v_cvt_pk_f16_f32 v140, v96, v97
	v_cvt_pk_f16_f32 v141, v98, v99
	ds_read_b64_tr_b16 v[152:153], v196 offset:28672
	ds_read_b64_tr_b16 v[154:155], v196 offset:29184
	v_add_f32_e32 v48, v102, v48
	v_add_f32_e32 v48, v103, v48
	v_add_f32_e32 v48, v104, v48
	v_add_f32_e32 v96, v105, v48
	s_waitcnt lgkmcnt(10)
	v_mfma_f32_32x32x16_f16 v[48:63], v[148:151], v[136:139], v[0:15]
	v_cvt_pk_f16_f32 v142, v100, v101
	v_cvt_pk_f16_f32 v143, v102, v103
	ds_read_b64_tr_b16 v[148:149], v196 offset:25600
	ds_read_b64_tr_b16 v[150:151], v196 offset:26112
	s_waitcnt lgkmcnt(11)
	v_mfma_f32_32x32x16_f16 v[64:79], v[176:179], v[128:131], v[64:79]
	v_add_f32_e32 v96, v106, v96
	v_add_f32_e32 v96, v107, v96
	v_add_f32_e32 v96, v108, v96
	v_add_f32_e32 v96, v109, v96
	v_cvt_pk_f16_f32 v132, v104, v105
	v_cvt_pk_f16_f32 v133, v106, v107
	ds_read_b64_tr_b16 v[100:101], v196 offset:29696
	ds_read_b64_tr_b16 v[102:103], v196 offset:30208
	s_waitcnt lgkmcnt(12)
	v_mfma_f32_32x32x16_f16 v[48:63], v[172:175], v[128:131], v[48:63]
	v_add_f32_e32 v96, v110, v96
	v_add_f32_e32 v96, v111, v96
	v_add_f32_e32 v96, v80, v96
	v_add_f32_e32 v104, v81, v96
	v_cvt_pk_f16_f32 v134, v108, v109
	v_cvt_pk_f16_f32 v135, v110, v111
	ds_read_b64_tr_b16 v[96:97], v196 offset:26624
	ds_read_b64_tr_b16 v[98:99], v196 offset:27136
	s_waitcnt lgkmcnt(13)
	v_mfma_f32_32x32x16_f16 v[64:79], v[168:171], v[120:123], v[64:79]
	v_add_f32_e32 v104, v82, v104
	v_add_f32_e32 v104, v83, v104
	v_add_f32_e32 v104, v84, v104
	v_add_f32_e32 v104, v85, v104
	v_cvt_pk_f16_f32 v124, v80, v81
	v_cvt_pk_f16_f32 v125, v82, v83
	ds_read_b64_tr_b16 v[80:81], v196 offset:30720
	ds_read_b64_tr_b16 v[82:83], v196 offset:31232
	s_waitcnt lgkmcnt(14)
	v_mfma_f32_32x32x16_f16 v[48:63], v[164:167], v[120:123], v[48:63]
	v_add_f32_e32 v104, v86, v104
	v_add_f32_e32 v104, v87, v104
	v_add_f32_e32 v104, v88, v104
	v_add_f32_e32 v104, v89, v104
	v_cvt_pk_f16_f32 v126, v84, v85
	v_cvt_pk_f16_f32 v127, v86, v87
	ds_read_b64_tr_b16 v[84:85], v196 offset:27648
	ds_read_b64_tr_b16 v[86:87], v196 offset:28160
	s_waitcnt lgkmcnt(14)
	v_mfma_f32_32x32x16_f16 v[64:79], v[160:163], v[112:115], v[64:79]
	v_add_f32_e32 v104, v90, v104
	v_add_f32_e32 v104, v91, v104
	v_add_f32_e32 v104, v92, v104
	v_add_f32_e32 v104, v93, v104
	v_cvt_pk_f16_f32 v116, v88, v89
	v_cvt_pk_f16_f32 v117, v90, v91
	ds_read_b64_tr_b16 v[88:89], v196 offset:31744
	ds_read_b64_tr_b16 v[90:91], v196 offset:32256
	v_mfma_f32_32x32x16_f16 v[48:63], v[156:159], v[112:115], v[48:63]
	v_add_f32_e32 v104, v94, v104
	v_add_f32_e32 v104, v95, v104
	v_cvt_pk_f16_f32 v118, v92, v93
	v_cvt_pk_f16_f32 v119, v94, v95
	v_lshl_add_u64 v[92:93], v[182:183], 0, s[4:5]
	s_add_i32 m0, s19, s25
	v_cmp_lt_f32_e32 vcc, s36, v104
	global_load_lds_dwordx4 v[92:93], off
	s_add_i32 m0, s18, s26
	v_lshl_add_u64 v[92:93], v[184:185], 0, s[12:13]
	global_load_lds_dwordx4 v[92:93], off
	s_cbranch_vccnz .Lmy_rare_2

.LBB2_5:
	s_add_i32 s14, s19, 0x2000
	s_cmpk_lg_i32 s19, 0x4000
	s_cselect_b32 s14, s14, 0
	s_waitcnt lgkmcnt(14)
	v_mfma_f32_32x32x16_f16 v[16:31], v[140:143], v[144:147], v[16:31]
	v_exp_f32_e32 v64, v64
	v_exp_f32_e32 v65, v65
	v_exp_f32_e32 v66, v66
	v_exp_f32_e32 v67, v67
	s_waitcnt lgkmcnt(12)
	v_mfma_f32_32x32x16_f16 v[32:47], v[140:143], v[152:155], v[32:47]
	v_exp_f32_e32 v68, v68
	v_exp_f32_e32 v69, v69
	v_exp_f32_e32 v70, v70
	v_exp_f32_e32 v71, v71
	v_add_u32_e32 v92, s14, v195
	ds_read_b128 v[172:175], v92
	ds_read_b128 v[168:171], v92 offset:512
	s_waitcnt lgkmcnt(12)
	v_mfma_f32_32x32x16_f16 v[16:31], v[132:135], v[148:151], v[16:31]
	v_exp_f32_e32 v72, v72
	v_exp_f32_e32 v73, v73
	v_exp_f32_e32 v74, v74
	v_exp_f32_e32 v75, v75
	ds_read_b128 v[164:167], v92 offset:2048
	ds_read_b128 v[160:163], v92 offset:2560
	s_waitcnt lgkmcnt(12)
	v_mfma_f32_32x32x16_f16 v[32:47], v[132:135], v[100:103], v[32:47]
	v_exp_f32_e32 v76, v76
	v_exp_f32_e32 v77, v77
	v_exp_f32_e32 v78, v78
	v_exp_f32_e32 v79, v79
	ds_read_b128 v[156:159], v92 offset:4096
	ds_read_b128 v[152:155], v92 offset:4608
	s_waitcnt lgkmcnt(12)
	v_mfma_f32_32x32x16_f16 v[16:31], v[124:127], v[96:99], v[16:31]
	v_exp_f32_e32 v48, v48
	v_exp_f32_e32 v49, v49
	v_exp_f32_e32 v50, v50
	v_exp_f32_e32 v51, v51
	ds_read_b128 v[148:151], v92 offset:6144
	ds_read_b128 v[144:147], v92 offset:6656
	s_waitcnt lgkmcnt(12)
	v_mfma_f32_32x32x16_f16 v[32:47], v[124:127], v[80:83], v[32:47]
	v_exp_f32_e32 v52, v52
	v_exp_f32_e32 v53, v53
	v_exp_f32_e32 v54, v54
	v_exp_f32_e32 v55, v55
	s_waitcnt lgkmcnt(10)
	v_mfma_f32_32x32x16_f16 v[16:31], v[116:119], v[84:87], v[16:31]
	v_exp_f32_e32 v56, v56
	v_exp_f32_e32 v57, v57
	v_exp_f32_e32 v58, v58
	v_exp_f32_e32 v59, v59
	s_waitcnt lgkmcnt(8)
	v_mfma_f32_32x32x16_f16 v[32:47], v[116:119], v[88:91], v[32:47]
	v_exp_f32_e32 v60, v60
	v_exp_f32_e32 v61, v61
	v_exp_f32_e32 v62, v62
	v_exp_f32_e32 v63, v63
	s_add_i32 s6, s14, 0x2000
	s_cmpk_lg_i32 s14, 0x4000
	s_cselect_b32 s19, s6, 0
	s_add_i32 s27, s27, 2
	v_lshl_add_u64 v[180:181], v[180:181], 0, s[2:3]
	v_lshl_add_u64 v[182:183], v[182:183], 0, s[2:3]
	v_lshl_add_u64 v[184:185], v[184:185], 0, s[2:3]
	s_mov_b32 s15, s29
	s_mov_b32 s31, s28
	s_mov_b32 s29, s18
	s_mov_b32 s28, s17
	s_cmp_gt_u32 s27, 28
	s_waitcnt vmcnt(3) lgkmcnt(0)
	s_barrier
	s_cbranch_scc0 .LBB2_1
